# combo5 + merge-phase gate hook rewritten: gate loads batched (one wait per 16 steps) instead of load-wait per element
# speedup vs baseline: 1.0181x; 1.0015x over previous
; __device__ __forceinline__ unsigned cvtpk(float lo, float hi) { f32x2_t v = {lo, hi}; bf16x2_t b = __builtin_convertvector(v, bf16x2_t); return __builtin_bit_cast(unsigned, b); }
; __device__ __forceinline__ float bflo(unsigned w) { return __uint_as_float(w << 16); }
; __device__ __forceinline__ float bfhi(unsigned w) { return __uint_as_float(w & 0xffff0000u); }
; __device__ __forceinline__ void phase_merge(const Ptrs& p, LAS unsigned char* lds) {
;     ...
;                 for (int m = 0; m < 4; ++m) { const int row = row0 + ai * 128 + wr * 64 + m * 16 + fr;
; #pragma unroll
;                     for (int bj = 0; bj < 2; ++bj)
; #pragma unroll
;                         for (int n = 0; n < 2; ++n) { const int c = col0 + bj * 128 + wc * 32 + n * 16 + fq * 4; const size_t o = (size_t)row * PLD + c;
;                             const u32x2 sa = *(const u32x2*)(pr + o + C_GA); u32x2 sc = sa; if (seg == 0) sc = *(const u32x2*)(pr + o + C_GC);
;                             f32x4 v = acc[ai][bj][m][n];
;                             const float a0 = bflo(sa.x), a1 = bfhi(sa.x), a2 = bflo(sa.y), a3 = bfhi(sa.y);
;                             if (seg == 0) { v[0] *= bflo(sc.x) * __builtin_amdgcn_rcpf(a0); v[1] *= bfhi(sc.x) * __builtin_amdgcn_rcpf(a1); v[2] *= bflo(sc.y) * __builtin_amdgcn_rcpf(a2); v[3] *= bfhi(sc.y) * __builtin_amdgcn_rcpf(a3); }
;                             else { v[0] *= a0; v[1] *= a1; v[2] *= a2; v[3] *= a3; }
;                             acc[ai][bj][m][n] = v;
;                             if (seg == 1) { u32x2 w; w.x = cvtpk(v[0], v[1]); w.y = cvtpk(v[2], v[3]); *(u32x2*)(mg + (size_t)row * D + c) = w; } }
;                     asm volatile("" ::: "memory"); }
.LBB0_525:
	v_mov_b32_e32 v2, v0
	s_nop 0
	v_ashrrev_i32_e32 v4, 2, v2
	v_and_b32_e32 v4, 0xffffffc0, v4
	v_and_or_b32 v5, v2, 15, s82
	v_add_u32_e32 v136, v5, v4
	v_lshrrev_b32_e32 v4, 1, v2
	v_lshrrev_b32_e32 v2, 2, v2
	v_and_b32_e32 v4, 0x60, v4
	v_and_b32_e32 v2, 12, v2
	v_or3_b32 v2, v2, v4, s75
	v_mov_b64_e32 v[4:5], s[10:11]
	v_mad_i64_i32 v[4:5], s[4:5], v136, s74, v[4:5]
	v_lshlrev_b32_e32 v2, 1, v2
	v_lshl_add_u64 v[138:139], v[4:5], 0, v[2:3]
	s_add_u32 s8, s10, 0x3800
	s_addc_u32 s9, s11, 0
	v_mov_b32_e32 v137, v136
	v_mov_b64_e32 v[212:213], s[8:9]
	v_mad_i64_i32 v[212:213], s[78:79], v137, s74, v[212:213]
	v_lshl_add_u64 v[212:213], v[212:213], 0, v[2:3]
	v_add_u32_e32 v137, 0x10, v136
	v_mov_b64_e32 v[214:215], s[8:9]
	v_mad_i64_i32 v[214:215], s[78:79], v137, s74, v[214:215]
	v_lshl_add_u64 v[214:215], v[214:215], 0, v[2:3]
	v_add_u32_e32 v137, 0x20, v136
	v_mov_b64_e32 v[216:217], s[8:9]
	v_mad_i64_i32 v[216:217], s[78:79], v137, s74, v[216:217]
	v_lshl_add_u64 v[216:217], v[216:217], 0, v[2:3]
	v_add_u32_e32 v137, 0x30, v136
	v_mov_b64_e32 v[218:219], s[8:9]
	v_mad_i64_i32 v[218:219], s[78:79], v137, s74, v[218:219]
	v_lshl_add_u64 v[218:219], v[218:219], 0, v[2:3]
	v_add_u32_e32 v137, 0x80, v136
	v_mov_b64_e32 v[220:221], s[8:9]
	v_mad_i64_i32 v[220:221], s[78:79], v137, s74, v[220:221]
	v_lshl_add_u64 v[220:221], v[220:221], 0, v[2:3]
	v_add_u32_e32 v137, 0x90, v136
	v_mov_b64_e32 v[222:223], s[8:9]
	v_mad_i64_i32 v[222:223], s[78:79], v137, s74, v[222:223]
	v_lshl_add_u64 v[222:223], v[222:223], 0, v[2:3]
	v_add_u32_e32 v137, 0xa0, v136
	v_mov_b64_e32 v[224:225], s[8:9]
	v_mad_i64_i32 v[224:225], s[78:79], v137, s74, v[224:225]
	v_lshl_add_u64 v[224:225], v[224:225], 0, v[2:3]
	v_add_u32_e32 v137, 0xb0, v136
	v_mov_b64_e32 v[226:227], s[8:9]
	v_mad_i64_i32 v[226:227], s[78:79], v137, s74, v[226:227]
	v_lshl_add_u64 v[226:227], v[226:227], 0, v[2:3]
	s_and_b64 vcc, exec, s[0:1]
	s_cbranch_vccnz .Lmy_mg_seg1
	global_load_dwordx2 v[148:149], v[212:213], off offset:2048
	global_load_dwordx2 v[150:151], v[212:213], off offset:-2048
	global_load_dwordx2 v[152:153], v[212:213], off offset:2080
	global_load_dwordx2 v[154:155], v[212:213], off offset:-2016
	global_load_dwordx2 v[156:157], v[212:213], off offset:2304
	global_load_dwordx2 v[158:159], v[212:213], off offset:-1792
	global_load_dwordx2 v[160:161], v[212:213], off offset:2336
	global_load_dwordx2 v[162:163], v[212:213], off offset:-1760
	global_load_dwordx2 v[164:165], v[214:215], off offset:2048
	global_load_dwordx2 v[166:167], v[214:215], off offset:-2048
	global_load_dwordx2 v[168:169], v[214:215], off offset:2080
	global_load_dwordx2 v[170:171], v[214:215], off offset:-2016
	global_load_dwordx2 v[172:173], v[214:215], off offset:2304
	global_load_dwordx2 v[174:175], v[214:215], off offset:-1792
	global_load_dwordx2 v[176:177], v[214:215], off offset:2336
	global_load_dwordx2 v[178:179], v[214:215], off offset:-1760
	global_load_dwordx2 v[180:181], v[216:217], off offset:2048
	global_load_dwordx2 v[182:183], v[216:217], off offset:-2048
	global_load_dwordx2 v[184:185], v[216:217], off offset:2080
	global_load_dwordx2 v[186:187], v[216:217], off offset:-2016
	global_load_dwordx2 v[188:189], v[216:217], off offset:2304
	global_load_dwordx2 v[190:191], v[216:217], off offset:-1792
	global_load_dwordx2 v[192:193], v[216:217], off offset:2336
	global_load_dwordx2 v[194:195], v[216:217], off offset:-1760
	global_load_dwordx2 v[196:197], v[218:219], off offset:2048
	global_load_dwordx2 v[198:199], v[218:219], off offset:-2048
	global_load_dwordx2 v[200:201], v[218:219], off offset:2080
	global_load_dwordx2 v[202:203], v[218:219], off offset:-2016
	global_load_dwordx2 v[204:205], v[218:219], off offset:2304
	global_load_dwordx2 v[206:207], v[218:219], off offset:-1792
	global_load_dwordx2 v[208:209], v[218:219], off offset:2336
	global_load_dwordx2 v[210:211], v[218:219], off offset:-1760
	s_waitcnt vmcnt(0)
	v_lshlrev_b32_e32 v140, 16, v148
	v_and_b32_e32 v141, 0xffff0000, v148
	v_lshlrev_b32_e32 v142, 16, v149
	v_and_b32_e32 v143, 0xffff0000, v149
	v_rcp_f32_e32 v140, v140
	v_rcp_f32_e32 v141, v141
	v_rcp_f32_e32 v142, v142
	v_rcp_f32_e32 v143, v143
	v_lshlrev_b32_e32 v144, 16, v150
	v_and_b32_e32 v145, 0xffff0000, v150
	v_lshlrev_b32_e32 v146, 16, v151
	v_and_b32_e32 v147, 0xffff0000, v151
	v_mul_f32_e32 v140, v140, v144
	v_mul_f32_e32 v141, v141, v145
	v_mul_f32_e32 v142, v142, v146
	v_mul_f32_e32 v143, v143, v147
	v_mul_f32_e32 v4, v8, v140
	v_mul_f32_e32 v5, v9, v141
	v_mul_f32_e32 v6, v10, v142
	v_mul_f32_e32 v7, v11, v143
	v_lshlrev_b32_e32 v140, 16, v152
	v_and_b32_e32 v141, 0xffff0000, v152
	v_lshlrev_b32_e32 v142, 16, v153
	v_and_b32_e32 v143, 0xffff0000, v153
	v_rcp_f32_e32 v140, v140
	v_rcp_f32_e32 v141, v141
	v_rcp_f32_e32 v142, v142
	v_rcp_f32_e32 v143, v143
	v_lshlrev_b32_e32 v144, 16, v154
	v_and_b32_e32 v145, 0xffff0000, v154
	v_lshlrev_b32_e32 v146, 16, v155
	v_and_b32_e32 v147, 0xffff0000, v155
	v_mul_f32_e32 v140, v140, v144
	v_mul_f32_e32 v141, v141, v145
	v_mul_f32_e32 v142, v142, v146
	v_mul_f32_e32 v143, v143, v147
	v_mul_f32_e32 v8, v12, v140
	v_mul_f32_e32 v9, v13, v141
	v_mul_f32_e32 v10, v14, v142
	v_mul_f32_e32 v11, v15, v143
	v_lshlrev_b32_e32 v140, 16, v156
	v_and_b32_e32 v141, 0xffff0000, v156
	v_lshlrev_b32_e32 v142, 16, v157
	v_and_b32_e32 v143, 0xffff0000, v157
	v_rcp_f32_e32 v140, v140
	v_rcp_f32_e32 v141, v141
	v_rcp_f32_e32 v142, v142
	v_rcp_f32_e32 v143, v143
	v_lshlrev_b32_e32 v144, 16, v158
	v_and_b32_e32 v145, 0xffff0000, v158
	v_lshlrev_b32_e32 v146, 16, v159
	v_and_b32_e32 v147, 0xffff0000, v159
	v_mul_f32_e32 v140, v140, v144
; __device__ __forceinline__ unsigned cvtpk(float lo, float hi) { f32x2_t v = {lo, hi}; bf16x2_t b = __builtin_convertvector(v, bf16x2_t); return __builtin_bit_cast(unsigned, b); }
; __device__ __forceinline__ float bflo(unsigned w) { return __uint_as_float(w << 16); }
; __device__ __forceinline__ float bfhi(unsigned w) { return __uint_as_float(w & 0xffff0000u); }
; __device__ __forceinline__ void phase_merge(const Ptrs& p, LAS unsigned char* lds) {
;     ...
;                 for (int m = 0; m < 4; ++m) { const int row = row0 + ai * 128 + wr * 64 + m * 16 + fr;
; #pragma unroll
;                     for (int bj = 0; bj < 2; ++bj)
; #pragma unroll
;                         for (int n = 0; n < 2; ++n) { const int c = col0 + bj * 128 + wc * 32 + n * 16 + fq * 4; const size_t o = (size_t)row * PLD + c;
;                             const u32x2 sa = *(const u32x2*)(pr + o + C_GA); u32x2 sc = sa; if (seg == 0) sc = *(const u32x2*)(pr + o + C_GC);
;                             f32x4 v = acc[ai][bj][m][n];
;                             const float a0 = bflo(sa.x), a1 = bfhi(sa.x), a2 = bflo(sa.y), a3 = bfhi(sa.y);
;                             if (seg == 0) { v[0] *= bflo(sc.x) * __builtin_amdgcn_rcpf(a0); v[1] *= bfhi(sc.x) * __builtin_amdgcn_rcpf(a1); v[2] *= bflo(sc.y) * __builtin_amdgcn_rcpf(a2); v[3] *= bfhi(sc.y) * __builtin_amdgcn_rcpf(a3); }
;                             else { v[0] *= a0; v[1] *= a1; v[2] *= a2; v[3] *= a3; }
;                             acc[ai][bj][m][n] = v;
;                             if (seg == 1) { u32x2 w; w.x = cvtpk(v[0], v[1]); w.y = cvtpk(v[2], v[3]); *(u32x2*)(mg + (size_t)row * D + c) = w; } }
;                     asm volatile("" ::: "memory"); }
	v_mul_f32_e32 v141, v141, v145
	v_mul_f32_e32 v142, v142, v146
	v_mul_f32_e32 v143, v143, v147
	v_mul_f32_e32 v12, v16, v140
	v_mul_f32_e32 v13, v17, v141
	v_mul_f32_e32 v14, v18, v142
	v_mul_f32_e32 v15, v19, v143
	v_lshlrev_b32_e32 v140, 16, v160
	v_and_b32_e32 v141, 0xffff0000, v160
	v_lshlrev_b32_e32 v142, 16, v161
	v_and_b32_e32 v143, 0xffff0000, v161
	v_rcp_f32_e32 v140, v140
	v_rcp_f32_e32 v141, v141
	v_rcp_f32_e32 v142, v142
	v_rcp_f32_e32 v143, v143
	v_lshlrev_b32_e32 v144, 16, v162
	v_and_b32_e32 v145, 0xffff0000, v162
	v_lshlrev_b32_e32 v146, 16, v163
	v_and_b32_e32 v147, 0xffff0000, v163
	v_mul_f32_e32 v140, v140, v144
	v_mul_f32_e32 v141, v141, v145
	v_mul_f32_e32 v142, v142, v146
	v_mul_f32_e32 v143, v143, v147
	v_mul_f32_e32 v16, v24, v140
	v_mul_f32_e32 v17, v25, v141
	v_mul_f32_e32 v18, v26, v142
	v_mul_f32_e32 v19, v27, v143
	v_lshlrev_b32_e32 v140, 16, v164
	v_and_b32_e32 v141, 0xffff0000, v164
	v_lshlrev_b32_e32 v142, 16, v165
	v_and_b32_e32 v143, 0xffff0000, v165
	v_rcp_f32_e32 v140, v140
	v_rcp_f32_e32 v141, v141
	v_rcp_f32_e32 v142, v142
	v_rcp_f32_e32 v143, v143
	v_lshlrev_b32_e32 v144, 16, v166
	v_and_b32_e32 v145, 0xffff0000, v166
	v_lshlrev_b32_e32 v146, 16, v167
	v_and_b32_e32 v147, 0xffff0000, v167
	v_mul_f32_e32 v140, v140, v144
	v_mul_f32_e32 v141, v141, v145
	v_mul_f32_e32 v142, v142, v146
	v_mul_f32_e32 v143, v143, v147
	v_mul_f32_e32 v24, v36, v140
	v_mul_f32_e32 v25, v37, v141
	v_mul_f32_e32 v26, v38, v142
	v_mul_f32_e32 v27, v39, v143
	v_lshlrev_b32_e32 v140, 16, v168
	v_and_b32_e32 v141, 0xffff0000, v168
	v_lshlrev_b32_e32 v142, 16, v169
	v_and_b32_e32 v143, 0xffff0000, v169
	v_rcp_f32_e32 v140, v140
	v_rcp_f32_e32 v141, v141
	v_rcp_f32_e32 v142, v142
	v_rcp_f32_e32 v143, v143
	v_lshlrev_b32_e32 v144, 16, v170
	v_and_b32_e32 v145, 0xffff0000, v170
	v_lshlrev_b32_e32 v146, 16, v171
	v_and_b32_e32 v147, 0xffff0000, v171
	v_mul_f32_e32 v140, v140, v144
	v_mul_f32_e32 v141, v141, v145
	v_mul_f32_e32 v142, v142, v146
	v_mul_f32_e32 v143, v143, v147
	v_mul_f32_e32 v36, v40, v140
	v_mul_f32_e32 v37, v41, v141
	v_mul_f32_e32 v38, v42, v142
	v_mul_f32_e32 v39, v43, v143
	v_lshlrev_b32_e32 v140, 16, v172
	v_and_b32_e32 v141, 0xffff0000, v172
	v_lshlrev_b32_e32 v142, 16, v173
	v_and_b32_e32 v143, 0xffff0000, v173
	v_rcp_f32_e32 v140, v140
	v_rcp_f32_e32 v141, v141
	v_rcp_f32_e32 v142, v142
	v_rcp_f32_e32 v143, v143
	v_lshlrev_b32_e32 v144, 16, v174
	v_and_b32_e32 v145, 0xffff0000, v174
	v_lshlrev_b32_e32 v146, 16, v175
	v_and_b32_e32 v147, 0xffff0000, v175
	v_mul_f32_e32 v140, v140, v144
	v_mul_f32_e32 v141, v141, v145
	v_mul_f32_e32 v142, v142, v146
	v_mul_f32_e32 v143, v143, v147
	v_mul_f32_e32 v40, v48, v140
	v_mul_f32_e32 v41, v49, v141
	v_mul_f32_e32 v42, v50, v142
	v_mul_f32_e32 v43, v51, v143
	v_lshlrev_b32_e32 v140, 16, v176
	v_and_b32_e32 v141, 0xffff0000, v176
	v_lshlrev_b32_e32 v142, 16, v177
	v_and_b32_e32 v143, 0xffff0000, v177
	v_rcp_f32_e32 v140, v140
	v_rcp_f32_e32 v141, v141
	v_rcp_f32_e32 v142, v142
	v_rcp_f32_e32 v143, v143
	v_lshlrev_b32_e32 v144, 16, v178
	v_and_b32_e32 v145, 0xffff0000, v178
	v_lshlrev_b32_e32 v146, 16, v179
	v_and_b32_e32 v147, 0xffff0000, v179
	v_mul_f32_e32 v140, v140, v144
	v_mul_f32_e32 v141, v141, v145
	v_mul_f32_e32 v142, v142, v146
	v_mul_f32_e32 v143, v143, v147
	v_mul_f32_e32 v48, v56, v140
	v_mul_f32_e32 v49, v57, v141
	v_mul_f32_e32 v50, v58, v142
	v_mul_f32_e32 v51, v59, v143
	v_lshlrev_b32_e32 v140, 16, v180
	v_and_b32_e32 v141, 0xffff0000, v180
	v_lshlrev_b32_e32 v142, 16, v181
	v_and_b32_e32 v143, 0xffff0000, v181
	v_rcp_f32_e32 v140, v140
	v_rcp_f32_e32 v141, v141
	v_rcp_f32_e32 v142, v142
	v_rcp_f32_e32 v143, v143
	v_lshlrev_b32_e32 v144, 16, v182
	v_and_b32_e32 v145, 0xffff0000, v182
	v_lshlrev_b32_e32 v146, 16, v183
	v_and_b32_e32 v147, 0xffff0000, v183
	v_mul_f32_e32 v140, v140, v144
	v_mul_f32_e32 v141, v141, v145
	v_mul_f32_e32 v142, v142, v146
	v_mul_f32_e32 v143, v143, v147
	v_mul_f32_e32 v56, v68, v140
	v_mul_f32_e32 v57, v69, v141
	v_mul_f32_e32 v58, v70, v142
	v_mul_f32_e32 v59, v71, v143
	v_lshlrev_b32_e32 v140, 16, v184
	v_and_b32_e32 v141, 0xffff0000, v184
	v_lshlrev_b32_e32 v142, 16, v185
	v_and_b32_e32 v143, 0xffff0000, v185
	v_rcp_f32_e32 v140, v140
	v_rcp_f32_e32 v141, v141
	v_rcp_f32_e32 v142, v142
	v_rcp_f32_e32 v143, v143
	v_lshlrev_b32_e32 v144, 16, v186
	v_and_b32_e32 v145, 0xffff0000, v186
	v_lshlrev_b32_e32 v146, 16, v187
	v_and_b32_e32 v147, 0xffff0000, v187
	v_mul_f32_e32 v140, v140, v144
	v_mul_f32_e32 v141, v141, v145
	v_mul_f32_e32 v142, v142, v146
	v_mul_f32_e32 v143, v143, v147
	v_mul_f32_e32 v68, v72, v140
	v_mul_f32_e32 v69, v73, v141
	v_mul_f32_e32 v70, v74, v142
	v_mul_f32_e32 v71, v75, v143
	v_lshlrev_b32_e32 v140, 16, v188
	v_and_b32_e32 v141, 0xffff0000, v188
	v_lshlrev_b32_e32 v142, 16, v189
	v_and_b32_e32 v143, 0xffff0000, v189
	v_rcp_f32_e32 v140, v140
	v_rcp_f32_e32 v141, v141
	v_rcp_f32_e32 v142, v142
	v_rcp_f32_e32 v143, v143
	v_lshlrev_b32_e32 v144, 16, v190
	v_and_b32_e32 v145, 0xffff0000, v190
	v_lshlrev_b32_e32 v146, 16, v191
	v_and_b32_e32 v147, 0xffff0000, v191
	v_mul_f32_e32 v140, v140, v144
	v_mul_f32_e32 v141, v141, v145
	v_mul_f32_e32 v142, v142, v146
	v_mul_f32_e32 v143, v143, v147
	v_mul_f32_e32 v72, v80, v140
	v_mul_f32_e32 v73, v81, v141
	v_mul_f32_e32 v74, v82, v142
	v_mul_f32_e32 v75, v83, v143
	v_lshlrev_b32_e32 v140, 16, v192
	v_and_b32_e32 v141, 0xffff0000, v192
	v_lshlrev_b32_e32 v142, 16, v193
	v_and_b32_e32 v143, 0xffff0000, v193
	v_rcp_f32_e32 v140, v140
	v_rcp_f32_e32 v141, v141
	v_rcp_f32_e32 v142, v142
	v_rcp_f32_e32 v143, v143
	v_lshlrev_b32_e32 v144, 16, v194
	v_and_b32_e32 v145, 0xffff0000, v194
; __device__ __forceinline__ unsigned cvtpk(float lo, float hi) { f32x2_t v = {lo, hi}; bf16x2_t b = __builtin_convertvector(v, bf16x2_t); return __builtin_bit_cast(unsigned, b); }
; __device__ __forceinline__ float bflo(unsigned w) { return __uint_as_float(w << 16); }
; __device__ __forceinline__ float bfhi(unsigned w) { return __uint_as_float(w & 0xffff0000u); }
; __device__ __forceinline__ void phase_merge(const Ptrs& p, LAS unsigned char* lds) {
;     ...
;                 for (int m = 0; m < 4; ++m) { const int row = row0 + ai * 128 + wr * 64 + m * 16 + fr;
; #pragma unroll
;                     for (int bj = 0; bj < 2; ++bj)
; #pragma unroll
;                         for (int n = 0; n < 2; ++n) { const int c = col0 + bj * 128 + wc * 32 + n * 16 + fq * 4; const size_t o = (size_t)row * PLD + c;
;                             const u32x2 sa = *(const u32x2*)(pr + o + C_GA); u32x2 sc = sa; if (seg == 0) sc = *(const u32x2*)(pr + o + C_GC);
;                             f32x4 v = acc[ai][bj][m][n];
;                             const float a0 = bflo(sa.x), a1 = bfhi(sa.x), a2 = bflo(sa.y), a3 = bfhi(sa.y);
;                             if (seg == 0) { v[0] *= bflo(sc.x) * __builtin_amdgcn_rcpf(a0); v[1] *= bfhi(sc.x) * __builtin_amdgcn_rcpf(a1); v[2] *= bflo(sc.y) * __builtin_amdgcn_rcpf(a2); v[3] *= bfhi(sc.y) * __builtin_amdgcn_rcpf(a3); }
;                             else { v[0] *= a0; v[1] *= a1; v[2] *= a2; v[3] *= a3; }
;                             acc[ai][bj][m][n] = v;
;                             if (seg == 1) { u32x2 w; w.x = cvtpk(v[0], v[1]); w.y = cvtpk(v[2], v[3]); *(u32x2*)(mg + (size_t)row * D + c) = w; } }
;                     asm volatile("" ::: "memory"); }
	v_lshlrev_b32_e32 v146, 16, v195
	v_and_b32_e32 v147, 0xffff0000, v195
	v_mul_f32_e32 v140, v140, v144
	v_mul_f32_e32 v141, v141, v145
	v_mul_f32_e32 v142, v142, v146
	v_mul_f32_e32 v143, v143, v147
	v_mul_f32_e32 v80, v88, v140
	v_mul_f32_e32 v81, v89, v141
	v_mul_f32_e32 v82, v90, v142
	v_mul_f32_e32 v83, v91, v143
	v_lshlrev_b32_e32 v140, 16, v196
	v_and_b32_e32 v141, 0xffff0000, v196
	v_lshlrev_b32_e32 v142, 16, v197
	v_and_b32_e32 v143, 0xffff0000, v197
	v_rcp_f32_e32 v140, v140
	v_rcp_f32_e32 v141, v141
	v_rcp_f32_e32 v142, v142
	v_rcp_f32_e32 v143, v143
	v_lshlrev_b32_e32 v144, 16, v198
	v_and_b32_e32 v145, 0xffff0000, v198
	v_lshlrev_b32_e32 v146, 16, v199
	v_and_b32_e32 v147, 0xffff0000, v199
	v_mul_f32_e32 v140, v140, v144
	v_mul_f32_e32 v141, v141, v145
	v_mul_f32_e32 v142, v142, v146
	v_mul_f32_e32 v143, v143, v147
	v_mul_f32_e32 v88, v100, v140
	v_mul_f32_e32 v89, v101, v141
	v_mul_f32_e32 v90, v102, v142
	v_mul_f32_e32 v91, v103, v143
	v_lshlrev_b32_e32 v140, 16, v200
	v_and_b32_e32 v141, 0xffff0000, v200
	v_lshlrev_b32_e32 v142, 16, v201
	v_and_b32_e32 v143, 0xffff0000, v201
	v_rcp_f32_e32 v140, v140
	v_rcp_f32_e32 v141, v141
	v_rcp_f32_e32 v142, v142
	v_rcp_f32_e32 v143, v143
	v_lshlrev_b32_e32 v144, 16, v202
	v_and_b32_e32 v145, 0xffff0000, v202
	v_lshlrev_b32_e32 v146, 16, v203
	v_and_b32_e32 v147, 0xffff0000, v203
	v_mul_f32_e32 v140, v140, v144
	v_mul_f32_e32 v141, v141, v145
	v_mul_f32_e32 v142, v142, v146
	v_mul_f32_e32 v143, v143, v147
	v_mul_f32_e32 v100, v104, v140
	v_mul_f32_e32 v101, v105, v141
	v_mul_f32_e32 v102, v106, v142
	v_mul_f32_e32 v103, v107, v143
	v_lshlrev_b32_e32 v140, 16, v204
	v_and_b32_e32 v141, 0xffff0000, v204
	v_lshlrev_b32_e32 v142, 16, v205
	v_and_b32_e32 v143, 0xffff0000, v205
	v_rcp_f32_e32 v140, v140
	v_rcp_f32_e32 v141, v141
	v_rcp_f32_e32 v142, v142
	v_rcp_f32_e32 v143, v143
	v_lshlrev_b32_e32 v144, 16, v206
	v_and_b32_e32 v145, 0xffff0000, v206
	v_lshlrev_b32_e32 v146, 16, v207
	v_and_b32_e32 v147, 0xffff0000, v207
	v_mul_f32_e32 v140, v140, v144
	v_mul_f32_e32 v141, v141, v145
	v_mul_f32_e32 v142, v142, v146
	v_mul_f32_e32 v143, v143, v147
	v_mul_f32_e32 v104, v112, v140
	v_mul_f32_e32 v105, v113, v141
	v_mul_f32_e32 v106, v114, v142
	v_mul_f32_e32 v107, v115, v143
	v_lshlrev_b32_e32 v140, 16, v208
	v_and_b32_e32 v141, 0xffff0000, v208
	v_lshlrev_b32_e32 v142, 16, v209
	v_and_b32_e32 v143, 0xffff0000, v209
	v_rcp_f32_e32 v140, v140
	v_rcp_f32_e32 v141, v141
	v_rcp_f32_e32 v142, v142
	v_rcp_f32_e32 v143, v143
	v_lshlrev_b32_e32 v144, 16, v210
	v_and_b32_e32 v145, 0xffff0000, v210
	v_lshlrev_b32_e32 v146, 16, v211
	v_and_b32_e32 v147, 0xffff0000, v211
	v_mul_f32_e32 v140, v140, v144
	v_mul_f32_e32 v141, v141, v145
	v_mul_f32_e32 v142, v142, v146
	v_mul_f32_e32 v143, v143, v147
	v_mul_f32_e32 v112, v120, v140
	v_mul_f32_e32 v113, v121, v141
	v_mul_f32_e32 v114, v122, v142
	v_mul_f32_e32 v115, v123, v143
	global_load_dwordx2 v[148:149], v[220:221], off offset:2048
	global_load_dwordx2 v[150:151], v[220:221], off offset:-2048
	global_load_dwordx2 v[152:153], v[220:221], off offset:2080
	global_load_dwordx2 v[154:155], v[220:221], off offset:-2016
	global_load_dwordx2 v[156:157], v[220:221], off offset:2304
	global_load_dwordx2 v[158:159], v[220:221], off offset:-1792
	global_load_dwordx2 v[160:161], v[220:221], off offset:2336
	global_load_dwordx2 v[162:163], v[220:221], off offset:-1760
	global_load_dwordx2 v[164:165], v[222:223], off offset:2048
	global_load_dwordx2 v[166:167], v[222:223], off offset:-2048
	global_load_dwordx2 v[168:169], v[222:223], off offset:2080
	global_load_dwordx2 v[170:171], v[222:223], off offset:-2016
	global_load_dwordx2 v[172:173], v[222:223], off offset:2304
	global_load_dwordx2 v[174:175], v[222:223], off offset:-1792
	global_load_dwordx2 v[176:177], v[222:223], off offset:2336
	global_load_dwordx2 v[178:179], v[222:223], off offset:-1760
	global_load_dwordx2 v[180:181], v[224:225], off offset:2048
	global_load_dwordx2 v[182:183], v[224:225], off offset:-2048
	global_load_dwordx2 v[184:185], v[224:225], off offset:2080
	global_load_dwordx2 v[186:187], v[224:225], off offset:-2016
	global_load_dwordx2 v[188:189], v[224:225], off offset:2304
	global_load_dwordx2 v[190:191], v[224:225], off offset:-1792
	global_load_dwordx2 v[192:193], v[224:225], off offset:2336
	global_load_dwordx2 v[194:195], v[224:225], off offset:-1760
	global_load_dwordx2 v[196:197], v[226:227], off offset:2048
	global_load_dwordx2 v[198:199], v[226:227], off offset:-2048
	global_load_dwordx2 v[200:201], v[226:227], off offset:2080
	global_load_dwordx2 v[202:203], v[226:227], off offset:-2016
	global_load_dwordx2 v[204:205], v[226:227], off offset:2304
	global_load_dwordx2 v[206:207], v[226:227], off offset:-1792
	global_load_dwordx2 v[208:209], v[226:227], off offset:2336
	global_load_dwordx2 v[210:211], v[226:227], off offset:-1760
	s_waitcnt vmcnt(0)
; __device__ __forceinline__ unsigned cvtpk(float lo, float hi) { f32x2_t v = {lo, hi}; bf16x2_t b = __builtin_convertvector(v, bf16x2_t); return __builtin_bit_cast(unsigned, b); }
; __device__ __forceinline__ float bflo(unsigned w) { return __uint_as_float(w << 16); }
; __device__ __forceinline__ float bfhi(unsigned w) { return __uint_as_float(w & 0xffff0000u); }
; __device__ __forceinline__ void phase_merge(const Ptrs& p, LAS unsigned char* lds) {
;     ...
;                 for (int m = 0; m < 4; ++m) { const int row = row0 + ai * 128 + wr * 64 + m * 16 + fr;
; #pragma unroll
;                     for (int bj = 0; bj < 2; ++bj)
; #pragma unroll
;                         for (int n = 0; n < 2; ++n) { const int c = col0 + bj * 128 + wc * 32 + n * 16 + fq * 4; const size_t o = (size_t)row * PLD + c;
;                             const u32x2 sa = *(const u32x2*)(pr + o + C_GA); u32x2 sc = sa; if (seg == 0) sc = *(const u32x2*)(pr + o + C_GC);
;                             f32x4 v = acc[ai][bj][m][n];
;                             const float a0 = bflo(sa.x), a1 = bfhi(sa.x), a2 = bflo(sa.y), a3 = bfhi(sa.y);
;                             if (seg == 0) { v[0] *= bflo(sc.x) * __builtin_amdgcn_rcpf(a0); v[1] *= bfhi(sc.x) * __builtin_amdgcn_rcpf(a1); v[2] *= bflo(sc.y) * __builtin_amdgcn_rcpf(a2); v[3] *= bfhi(sc.y) * __builtin_amdgcn_rcpf(a3); }
;                             else { v[0] *= a0; v[1] *= a1; v[2] *= a2; v[3] *= a3; }
;                             acc[ai][bj][m][n] = v;
;                             if (seg == 1) { u32x2 w; w.x = cvtpk(v[0], v[1]); w.y = cvtpk(v[2], v[3]); *(u32x2*)(mg + (size_t)row * D + c) = w; } }
;                     asm volatile("" ::: "memory"); }
	v_lshlrev_b32_e32 v140, 16, v148
	v_and_b32_e32 v141, 0xffff0000, v148
	v_lshlrev_b32_e32 v142, 16, v149
	v_and_b32_e32 v143, 0xffff0000, v149
	v_rcp_f32_e32 v140, v140
	v_rcp_f32_e32 v141, v141
	v_rcp_f32_e32 v142, v142
	v_rcp_f32_e32 v143, v143
	v_lshlrev_b32_e32 v144, 16, v150
	v_and_b32_e32 v145, 0xffff0000, v150
	v_lshlrev_b32_e32 v146, 16, v151
	v_and_b32_e32 v147, 0xffff0000, v151
	v_mul_f32_e32 v140, v140, v144
	v_mul_f32_e32 v141, v141, v145
	v_mul_f32_e32 v142, v142, v146
	v_mul_f32_e32 v143, v143, v147
	v_mul_f32_e32 v120, v128, v140
	v_mul_f32_e32 v121, v129, v141
	v_mul_f32_e32 v122, v130, v142
	v_mul_f32_e32 v123, v131, v143
	v_lshlrev_b32_e32 v140, 16, v152
	v_and_b32_e32 v141, 0xffff0000, v152
	v_lshlrev_b32_e32 v142, 16, v153
	v_and_b32_e32 v143, 0xffff0000, v153
	v_rcp_f32_e32 v140, v140
	v_rcp_f32_e32 v141, v141
	v_rcp_f32_e32 v142, v142
	v_rcp_f32_e32 v143, v143
	v_lshlrev_b32_e32 v144, 16, v154
	v_and_b32_e32 v145, 0xffff0000, v154
	v_lshlrev_b32_e32 v146, 16, v155
	v_and_b32_e32 v147, 0xffff0000, v155
	v_mul_f32_e32 v140, v140, v144
	v_mul_f32_e32 v141, v141, v145
	v_mul_f32_e32 v142, v142, v146
	v_mul_f32_e32 v143, v143, v147
	v_mul_f32_e32 v128, v132, v140
	v_mul_f32_e32 v129, v133, v141
	v_mul_f32_e32 v130, v134, v142
	v_mul_f32_e32 v131, v135, v143
	v_lshlrev_b32_e32 v140, 16, v156
	v_and_b32_e32 v141, 0xffff0000, v156
	v_lshlrev_b32_e32 v142, 16, v157
	v_and_b32_e32 v143, 0xffff0000, v157
	v_rcp_f32_e32 v140, v140
	v_rcp_f32_e32 v141, v141
	v_rcp_f32_e32 v142, v142
	v_rcp_f32_e32 v143, v143
	v_lshlrev_b32_e32 v144, 16, v158
	v_and_b32_e32 v145, 0xffff0000, v158
	v_lshlrev_b32_e32 v146, 16, v159
	v_and_b32_e32 v147, 0xffff0000, v159
	v_mul_f32_e32 v140, v140, v144
	v_mul_f32_e32 v141, v141, v145
	v_mul_f32_e32 v142, v142, v146
	v_mul_f32_e32 v143, v143, v147
	v_mul_f32_e32 v132, v124, v140
	v_mul_f32_e32 v133, v125, v141
	v_mul_f32_e32 v134, v126, v142
	v_mul_f32_e32 v135, v127, v143
	v_lshlrev_b32_e32 v140, 16, v160
	v_and_b32_e32 v141, 0xffff0000, v160
	v_lshlrev_b32_e32 v142, 16, v161
	v_and_b32_e32 v143, 0xffff0000, v161
	v_rcp_f32_e32 v140, v140
	v_rcp_f32_e32 v141, v141
	v_rcp_f32_e32 v142, v142
	v_rcp_f32_e32 v143, v143
	v_lshlrev_b32_e32 v144, 16, v162
	v_and_b32_e32 v145, 0xffff0000, v162
	v_lshlrev_b32_e32 v146, 16, v163
	v_and_b32_e32 v147, 0xffff0000, v163
	v_mul_f32_e32 v140, v140, v144
	v_mul_f32_e32 v141, v141, v145
	v_mul_f32_e32 v142, v142, v146
	v_mul_f32_e32 v143, v143, v147
	v_mul_f32_e32 v124, v116, v140
	v_mul_f32_e32 v125, v117, v141
	v_mul_f32_e32 v126, v118, v142
	v_mul_f32_e32 v127, v119, v143
	v_lshlrev_b32_e32 v140, 16, v164
	v_and_b32_e32 v141, 0xffff0000, v164
	v_lshlrev_b32_e32 v142, 16, v165
	v_and_b32_e32 v143, 0xffff0000, v165
	v_rcp_f32_e32 v140, v140
	v_rcp_f32_e32 v141, v141
	v_rcp_f32_e32 v142, v142
	v_rcp_f32_e32 v143, v143
	v_lshlrev_b32_e32 v144, 16, v166
	v_and_b32_e32 v145, 0xffff0000, v166
	v_lshlrev_b32_e32 v146, 16, v167
	v_and_b32_e32 v147, 0xffff0000, v167
	v_mul_f32_e32 v140, v140, v144
	v_mul_f32_e32 v141, v141, v145
	v_mul_f32_e32 v142, v142, v146
	v_mul_f32_e32 v143, v143, v147
	v_mul_f32_e32 v116, v108, v140
	v_mul_f32_e32 v117, v109, v141
	v_mul_f32_e32 v118, v110, v142
	v_mul_f32_e32 v119, v111, v143
	v_lshlrev_b32_e32 v140, 16, v168
	v_and_b32_e32 v141, 0xffff0000, v168
	v_lshlrev_b32_e32 v142, 16, v169
	v_and_b32_e32 v143, 0xffff0000, v169
	v_rcp_f32_e32 v140, v140
	v_rcp_f32_e32 v141, v141
	v_rcp_f32_e32 v142, v142
	v_rcp_f32_e32 v143, v143
	v_lshlrev_b32_e32 v144, 16, v170
	v_and_b32_e32 v145, 0xffff0000, v170
	v_lshlrev_b32_e32 v146, 16, v171
	v_and_b32_e32 v147, 0xffff0000, v171
	v_mul_f32_e32 v140, v140, v144
	v_mul_f32_e32 v141, v141, v145
	v_mul_f32_e32 v142, v142, v146
	v_mul_f32_e32 v143, v143, v147
	v_mul_f32_e32 v108, v96, v140
	v_mul_f32_e32 v109, v97, v141
	v_mul_f32_e32 v110, v98, v142
	v_mul_f32_e32 v111, v99, v143
	v_lshlrev_b32_e32 v140, 16, v172
	v_and_b32_e32 v141, 0xffff0000, v172
	v_lshlrev_b32_e32 v142, 16, v173
	v_and_b32_e32 v143, 0xffff0000, v173
	v_rcp_f32_e32 v140, v140
	v_rcp_f32_e32 v141, v141
	v_rcp_f32_e32 v142, v142
	v_rcp_f32_e32 v143, v143
	v_lshlrev_b32_e32 v144, 16, v174
	v_and_b32_e32 v145, 0xffff0000, v174
	v_lshlrev_b32_e32 v146, 16, v175
	v_and_b32_e32 v147, 0xffff0000, v175
	v_mul_f32_e32 v140, v140, v144
	v_mul_f32_e32 v141, v141, v145
	v_mul_f32_e32 v142, v142, v146
	v_mul_f32_e32 v143, v143, v147
	v_mul_f32_e32 v96, v92, v140
	v_mul_f32_e32 v97, v93, v141
	v_mul_f32_e32 v98, v94, v142
	v_mul_f32_e32 v99, v95, v143
	v_lshlrev_b32_e32 v140, 16, v176
	v_and_b32_e32 v141, 0xffff0000, v176
	v_lshlrev_b32_e32 v142, 16, v177
	v_and_b32_e32 v143, 0xffff0000, v177
	v_rcp_f32_e32 v140, v140
	v_rcp_f32_e32 v141, v141
	v_rcp_f32_e32 v142, v142
	v_rcp_f32_e32 v143, v143
	v_lshlrev_b32_e32 v144, 16, v178
	v_and_b32_e32 v145, 0xffff0000, v178
	v_lshlrev_b32_e32 v146, 16, v179
	v_and_b32_e32 v147, 0xffff0000, v179
	v_mul_f32_e32 v140, v140, v144
	v_mul_f32_e32 v141, v141, v145
	v_mul_f32_e32 v142, v142, v146
	v_mul_f32_e32 v143, v143, v147
	v_mul_f32_e32 v92, v84, v140
	v_mul_f32_e32 v93, v85, v141
	v_mul_f32_e32 v94, v86, v142
	v_mul_f32_e32 v95, v87, v143
	v_lshlrev_b32_e32 v140, 16, v180
	v_and_b32_e32 v141, 0xffff0000, v180
	v_lshlrev_b32_e32 v142, 16, v181
	v_and_b32_e32 v143, 0xffff0000, v181
	v_rcp_f32_e32 v140, v140
	v_rcp_f32_e32 v141, v141
	v_rcp_f32_e32 v142, v142
	v_rcp_f32_e32 v143, v143
	v_lshlrev_b32_e32 v144, 16, v182
	v_and_b32_e32 v145, 0xffff0000, v182
	v_lshlrev_b32_e32 v146, 16, v183
	v_and_b32_e32 v147, 0xffff0000, v183
	v_mul_f32_e32 v140, v140, v144
	v_mul_f32_e32 v141, v141, v145
	v_mul_f32_e32 v142, v142, v146
; __device__ __forceinline__ unsigned cvtpk(float lo, float hi) { f32x2_t v = {lo, hi}; bf16x2_t b = __builtin_convertvector(v, bf16x2_t); return __builtin_bit_cast(unsigned, b); }
; __device__ __forceinline__ float bflo(unsigned w) { return __uint_as_float(w << 16); }
; __device__ __forceinline__ float bfhi(unsigned w) { return __uint_as_float(w & 0xffff0000u); }
; __device__ __forceinline__ void phase_merge(const Ptrs& p, LAS unsigned char* lds) {
;     ...
;                 for (int m = 0; m < 4; ++m) { const int row = row0 + ai * 128 + wr * 64 + m * 16 + fr;
; #pragma unroll
;                     for (int bj = 0; bj < 2; ++bj)
; #pragma unroll
;                         for (int n = 0; n < 2; ++n) { const int c = col0 + bj * 128 + wc * 32 + n * 16 + fq * 4; const size_t o = (size_t)row * PLD + c;
;                             const u32x2 sa = *(const u32x2*)(pr + o + C_GA); u32x2 sc = sa; if (seg == 0) sc = *(const u32x2*)(pr + o + C_GC);
;                             f32x4 v = acc[ai][bj][m][n];
;                             const float a0 = bflo(sa.x), a1 = bfhi(sa.x), a2 = bflo(sa.y), a3 = bfhi(sa.y);
;                             if (seg == 0) { v[0] *= bflo(sc.x) * __builtin_amdgcn_rcpf(a0); v[1] *= bfhi(sc.x) * __builtin_amdgcn_rcpf(a1); v[2] *= bflo(sc.y) * __builtin_amdgcn_rcpf(a2); v[3] *= bfhi(sc.y) * __builtin_amdgcn_rcpf(a3); }
;                             else { v[0] *= a0; v[1] *= a1; v[2] *= a2; v[3] *= a3; }
;                             acc[ai][bj][m][n] = v;
;                             if (seg == 1) { u32x2 w; w.x = cvtpk(v[0], v[1]); w.y = cvtpk(v[2], v[3]); *(u32x2*)(mg + (size_t)row * D + c) = w; } }
;                     asm volatile("" ::: "memory"); }
	v_mul_f32_e32 v143, v143, v147
	v_mul_f32_e32 v84, v76, v140
	v_mul_f32_e32 v85, v77, v141
	v_mul_f32_e32 v86, v78, v142
	v_mul_f32_e32 v87, v79, v143
	v_lshlrev_b32_e32 v140, 16, v184
	v_and_b32_e32 v141, 0xffff0000, v184
	v_lshlrev_b32_e32 v142, 16, v185
	v_and_b32_e32 v143, 0xffff0000, v185
	v_rcp_f32_e32 v140, v140
	v_rcp_f32_e32 v141, v141
	v_rcp_f32_e32 v142, v142
	v_rcp_f32_e32 v143, v143
	v_lshlrev_b32_e32 v144, 16, v186
	v_and_b32_e32 v145, 0xffff0000, v186
	v_lshlrev_b32_e32 v146, 16, v187
	v_and_b32_e32 v147, 0xffff0000, v187
	v_mul_f32_e32 v140, v140, v144
	v_mul_f32_e32 v141, v141, v145
	v_mul_f32_e32 v142, v142, v146
	v_mul_f32_e32 v143, v143, v147
	v_mul_f32_e32 v76, v64, v140
	v_mul_f32_e32 v77, v65, v141
	v_mul_f32_e32 v78, v66, v142
	v_mul_f32_e32 v79, v67, v143
	v_lshlrev_b32_e32 v140, 16, v188
	v_and_b32_e32 v141, 0xffff0000, v188
	v_lshlrev_b32_e32 v142, 16, v189
	v_and_b32_e32 v143, 0xffff0000, v189
	v_rcp_f32_e32 v140, v140
	v_rcp_f32_e32 v141, v141
	v_rcp_f32_e32 v142, v142
	v_rcp_f32_e32 v143, v143
	v_lshlrev_b32_e32 v144, 16, v190
	v_and_b32_e32 v145, 0xffff0000, v190
	v_lshlrev_b32_e32 v146, 16, v191
	v_and_b32_e32 v147, 0xffff0000, v191
	v_mul_f32_e32 v140, v140, v144
	v_mul_f32_e32 v141, v141, v145
	v_mul_f32_e32 v142, v142, v146
	v_mul_f32_e32 v143, v143, v147
	v_mul_f32_e32 v64, v60, v140
	v_mul_f32_e32 v65, v61, v141
	v_mul_f32_e32 v66, v62, v142
	v_mul_f32_e32 v67, v63, v143
	v_lshlrev_b32_e32 v140, 16, v192
	v_and_b32_e32 v141, 0xffff0000, v192
	v_lshlrev_b32_e32 v142, 16, v193
	v_and_b32_e32 v143, 0xffff0000, v193
	v_rcp_f32_e32 v140, v140
	v_rcp_f32_e32 v141, v141
	v_rcp_f32_e32 v142, v142
	v_rcp_f32_e32 v143, v143
	v_lshlrev_b32_e32 v144, 16, v194
	v_and_b32_e32 v145, 0xffff0000, v194
	v_lshlrev_b32_e32 v146, 16, v195
	v_and_b32_e32 v147, 0xffff0000, v195
	v_mul_f32_e32 v140, v140, v144
	v_mul_f32_e32 v141, v141, v145
	v_mul_f32_e32 v142, v142, v146
	v_mul_f32_e32 v143, v143, v147
	v_mul_f32_e32 v60, v52, v140
	v_mul_f32_e32 v61, v53, v141
	v_mul_f32_e32 v62, v54, v142
	v_mul_f32_e32 v63, v55, v143
	v_lshlrev_b32_e32 v140, 16, v196
	v_and_b32_e32 v141, 0xffff0000, v196
	v_lshlrev_b32_e32 v142, 16, v197
	v_and_b32_e32 v143, 0xffff0000, v197
	v_rcp_f32_e32 v140, v140
	v_rcp_f32_e32 v141, v141
	v_rcp_f32_e32 v142, v142
	v_rcp_f32_e32 v143, v143
	v_lshlrev_b32_e32 v144, 16, v198
	v_and_b32_e32 v145, 0xffff0000, v198
	v_lshlrev_b32_e32 v146, 16, v199
	v_and_b32_e32 v147, 0xffff0000, v199
	v_mul_f32_e32 v140, v140, v144
	v_mul_f32_e32 v141, v141, v145
	v_mul_f32_e32 v142, v142, v146
	v_mul_f32_e32 v143, v143, v147
	v_mul_f32_e32 v52, v44, v140
	v_mul_f32_e32 v53, v45, v141
	v_mul_f32_e32 v54, v46, v142
	v_mul_f32_e32 v55, v47, v143
	v_lshlrev_b32_e32 v140, 16, v200
	v_and_b32_e32 v141, 0xffff0000, v200
	v_lshlrev_b32_e32 v142, 16, v201
	v_and_b32_e32 v143, 0xffff0000, v201
	v_rcp_f32_e32 v140, v140
	v_rcp_f32_e32 v141, v141
	v_rcp_f32_e32 v142, v142
	v_rcp_f32_e32 v143, v143
	v_lshlrev_b32_e32 v144, 16, v202
	v_and_b32_e32 v145, 0xffff0000, v202
	v_lshlrev_b32_e32 v146, 16, v203
	v_and_b32_e32 v147, 0xffff0000, v203
	v_mul_f32_e32 v140, v140, v144
	v_mul_f32_e32 v141, v141, v145
	v_mul_f32_e32 v142, v142, v146
	v_mul_f32_e32 v143, v143, v147
	v_mul_f32_e32 v44, v32, v140
	v_mul_f32_e32 v45, v33, v141
	v_mul_f32_e32 v46, v34, v142
	v_mul_f32_e32 v47, v35, v143
	v_lshlrev_b32_e32 v140, 16, v204
	v_and_b32_e32 v141, 0xffff0000, v204
	v_lshlrev_b32_e32 v142, 16, v205
	v_and_b32_e32 v143, 0xffff0000, v205
	v_rcp_f32_e32 v140, v140
	v_rcp_f32_e32 v141, v141
	v_rcp_f32_e32 v142, v142
	v_rcp_f32_e32 v143, v143
	v_lshlrev_b32_e32 v144, 16, v206
	v_and_b32_e32 v145, 0xffff0000, v206
	v_lshlrev_b32_e32 v146, 16, v207
	v_and_b32_e32 v147, 0xffff0000, v207
	v_mul_f32_e32 v140, v140, v144
	v_mul_f32_e32 v141, v141, v145
	v_mul_f32_e32 v142, v142, v146
	v_mul_f32_e32 v143, v143, v147
	v_mul_f32_e32 v32, v28, v140
	v_mul_f32_e32 v33, v29, v141
	v_mul_f32_e32 v34, v30, v142
	v_mul_f32_e32 v35, v31, v143
	v_lshlrev_b32_e32 v140, 16, v208
	v_and_b32_e32 v141, 0xffff0000, v208
	v_lshlrev_b32_e32 v142, 16, v209
	v_and_b32_e32 v143, 0xffff0000, v209
	v_rcp_f32_e32 v140, v140
	v_rcp_f32_e32 v141, v141
	v_rcp_f32_e32 v142, v142
	v_rcp_f32_e32 v143, v143
	v_lshlrev_b32_e32 v144, 16, v210
	v_and_b32_e32 v145, 0xffff0000, v210
	v_lshlrev_b32_e32 v146, 16, v211
	v_and_b32_e32 v147, 0xffff0000, v211
	v_mul_f32_e32 v140, v140, v144
	v_mul_f32_e32 v141, v141, v145
	v_mul_f32_e32 v142, v142, v146
	v_mul_f32_e32 v143, v143, v147
	v_mul_f32_e32 v28, v20, v140
	v_mul_f32_e32 v29, v21, v141
	v_mul_f32_e32 v30, v22, v142
	v_mul_f32_e32 v31, v23, v143
	s_branch .LBB0_510
; __device__ __forceinline__ unsigned cvtpk(float lo, float hi) { f32x2_t v = {lo, hi}; bf16x2_t b = __builtin_convertvector(v, bf16x2_t); return __builtin_bit_cast(unsigned, b); }
; __device__ __forceinline__ float bflo(unsigned w) { return __uint_as_float(w << 16); }
; __device__ __forceinline__ float bfhi(unsigned w) { return __uint_as_float(w & 0xffff0000u); }
; __device__ __forceinline__ void phase_merge(const Ptrs& p, LAS unsigned char* lds) {
;     ...
;                 for (int m = 0; m < 4; ++m) { const int row = row0 + ai * 128 + wr * 64 + m * 16 + fr;
; #pragma unroll
;                     for (int bj = 0; bj < 2; ++bj)
; #pragma unroll
;                         for (int n = 0; n < 2; ++n) { const int c = col0 + bj * 128 + wc * 32 + n * 16 + fq * 4; const size_t o = (size_t)row * PLD + c;
;                             const u32x2 sa = *(const u32x2*)(pr + o + C_GA); u32x2 sc = sa; if (seg == 0) sc = *(const u32x2*)(pr + o + C_GC);
;                             f32x4 v = acc[ai][bj][m][n];
;                             const float a0 = bflo(sa.x), a1 = bfhi(sa.x), a2 = bflo(sa.y), a3 = bfhi(sa.y);
;                             if (seg == 0) { v[0] *= bflo(sc.x) * __builtin_amdgcn_rcpf(a0); v[1] *= bfhi(sc.x) * __builtin_amdgcn_rcpf(a1); v[2] *= bflo(sc.y) * __builtin_amdgcn_rcpf(a2); v[3] *= bfhi(sc.y) * __builtin_amdgcn_rcpf(a3); }
;                             else { v[0] *= a0; v[1] *= a1; v[2] *= a2; v[3] *= a3; }
;                             acc[ai][bj][m][n] = v;
;                             if (seg == 1) { u32x2 w; w.x = cvtpk(v[0], v[1]); w.y = cvtpk(v[2], v[3]); *(u32x2*)(mg + (size_t)row * D + c) = w; } }
;                     asm volatile("" ::: "memory"); }
.Lmy_mg_seg1:
	global_load_dwordx2 v[148:149], v[212:213], off offset:2048
	global_load_dwordx2 v[150:151], v[212:213], off offset:2080
	global_load_dwordx2 v[152:153], v[212:213], off offset:2304
	global_load_dwordx2 v[154:155], v[212:213], off offset:2336
	global_load_dwordx2 v[156:157], v[214:215], off offset:2048
	global_load_dwordx2 v[158:159], v[214:215], off offset:2080
	global_load_dwordx2 v[160:161], v[214:215], off offset:2304
	global_load_dwordx2 v[162:163], v[214:215], off offset:2336
	global_load_dwordx2 v[164:165], v[216:217], off offset:2048
	global_load_dwordx2 v[166:167], v[216:217], off offset:2080
	global_load_dwordx2 v[168:169], v[216:217], off offset:2304
	global_load_dwordx2 v[170:171], v[216:217], off offset:2336
	global_load_dwordx2 v[172:173], v[218:219], off offset:2048
	global_load_dwordx2 v[174:175], v[218:219], off offset:2080
	global_load_dwordx2 v[176:177], v[218:219], off offset:2304
	global_load_dwordx2 v[178:179], v[218:219], off offset:2336
	global_load_dwordx2 v[180:181], v[220:221], off offset:2048
	global_load_dwordx2 v[182:183], v[220:221], off offset:2080
	global_load_dwordx2 v[184:185], v[220:221], off offset:2304
	global_load_dwordx2 v[186:187], v[220:221], off offset:2336
	global_load_dwordx2 v[188:189], v[222:223], off offset:2048
	global_load_dwordx2 v[190:191], v[222:223], off offset:2080
	global_load_dwordx2 v[192:193], v[222:223], off offset:2304
	global_load_dwordx2 v[194:195], v[222:223], off offset:2336
	global_load_dwordx2 v[196:197], v[224:225], off offset:2048
	global_load_dwordx2 v[198:199], v[224:225], off offset:2080
	global_load_dwordx2 v[200:201], v[224:225], off offset:2304
	global_load_dwordx2 v[202:203], v[224:225], off offset:2336
	global_load_dwordx2 v[204:205], v[226:227], off offset:2048
	global_load_dwordx2 v[206:207], v[226:227], off offset:2080
	global_load_dwordx2 v[208:209], v[226:227], off offset:2304
	global_load_dwordx2 v[210:211], v[226:227], off offset:2336
	v_mov_b32_e32 v139, 0
	v_mov_b32_e32 v138, v136
	v_lshlrev_b64 v[228:229], 12, v[138:139]
	v_lshl_add_u64 v[228:229], s[12:13], 0, v[228:229]
	v_lshl_add_u64 v[228:229], v[228:229], 0, v[2:3]
	v_add_u32_e32 v138, 0x10, v136
	v_lshlrev_b64 v[230:231], 12, v[138:139]
	v_lshl_add_u64 v[230:231], s[12:13], 0, v[230:231]
	v_lshl_add_u64 v[230:231], v[230:231], 0, v[2:3]
	v_add_u32_e32 v138, 0x20, v136
	v_lshlrev_b64 v[232:233], 12, v[138:139]
	v_lshl_add_u64 v[232:233], s[12:13], 0, v[232:233]
	v_lshl_add_u64 v[232:233], v[232:233], 0, v[2:3]
	v_add_u32_e32 v138, 0x30, v136
	v_lshlrev_b64 v[234:235], 12, v[138:139]
	v_lshl_add_u64 v[234:235], s[12:13], 0, v[234:235]
	v_lshl_add_u64 v[234:235], v[234:235], 0, v[2:3]
	v_add_u32_e32 v138, 0x80, v136
	v_lshlrev_b64 v[236:237], 12, v[138:139]
	v_lshl_add_u64 v[236:237], s[12:13], 0, v[236:237]
	v_lshl_add_u64 v[236:237], v[236:237], 0, v[2:3]
	v_add_u32_e32 v138, 0x90, v136
	v_lshlrev_b64 v[238:239], 12, v[138:139]
	v_lshl_add_u64 v[238:239], s[12:13], 0, v[238:239]
	v_lshl_add_u64 v[238:239], v[238:239], 0, v[2:3]
	v_add_u32_e32 v138, 0xa0, v136
	v_lshlrev_b64 v[240:241], 12, v[138:139]
	v_lshl_add_u64 v[240:241], s[12:13], 0, v[240:241]
	v_lshl_add_u64 v[240:241], v[240:241], 0, v[2:3]
	v_add_u32_e32 v138, 0xb0, v136
	v_lshlrev_b64 v[242:243], 12, v[138:139]
	v_lshl_add_u64 v[242:243], s[12:13], 0, v[242:243]
	v_lshl_add_u64 v[242:243], v[242:243], 0, v[2:3]
	s_waitcnt vmcnt(0)
	v_lshlrev_b32_e32 v140, 16, v148
	v_and_b32_e32 v141, 0xffff0000, v148
	v_lshlrev_b32_e32 v142, 16, v149
	v_and_b32_e32 v143, 0xffff0000, v149
	v_mul_f32_e32 v4, v8, v140
	v_mul_f32_e32 v5, v9, v141
	v_mul_f32_e32 v6, v10, v142
	v_mul_f32_e32 v7, v11, v143
	v_cvt_pk_bf16_f32 v144, v4, v5
	v_cvt_pk_bf16_f32 v145, v6, v7
	global_store_dwordx2 v[228:229], v[144:145], off
	v_lshlrev_b32_e32 v140, 16, v150
	v_and_b32_e32 v141, 0xffff0000, v150
	v_lshlrev_b32_e32 v142, 16, v151
	v_and_b32_e32 v143, 0xffff0000, v151
	v_mul_f32_e32 v8, v12, v140
	v_mul_f32_e32 v9, v13, v141
	v_mul_f32_e32 v10, v14, v142
	v_mul_f32_e32 v11, v15, v143
	v_cvt_pk_bf16_f32 v146, v8, v9
	v_cvt_pk_bf16_f32 v147, v10, v11
	global_store_dwordx2 v[228:229], v[146:147], off offset:32
	v_lshlrev_b32_e32 v140, 16, v152
	v_and_b32_e32 v141, 0xffff0000, v152
	v_lshlrev_b32_e32 v142, 16, v153
	v_and_b32_e32 v143, 0xffff0000, v153
	v_mul_f32_e32 v12, v16, v140
	v_mul_f32_e32 v13, v17, v141
	v_mul_f32_e32 v14, v18, v142
	v_mul_f32_e32 v15, v19, v143
	v_cvt_pk_bf16_f32 v144, v12, v13
	v_cvt_pk_bf16_f32 v145, v14, v15
	global_store_dwordx2 v[228:229], v[144:145], off offset:256
	v_lshlrev_b32_e32 v140, 16, v154
	v_and_b32_e32 v141, 0xffff0000, v154
	v_lshlrev_b32_e32 v142, 16, v155
	v_and_b32_e32 v143, 0xffff0000, v155
	v_mul_f32_e32 v16, v24, v140
	v_mul_f32_e32 v17, v25, v141
	v_mul_f32_e32 v18, v26, v142
	v_mul_f32_e32 v19, v27, v143
	v_cvt_pk_bf16_f32 v146, v16, v17
	v_cvt_pk_bf16_f32 v147, v18, v19
	global_store_dwordx2 v[228:229], v[146:147], off offset:288
	v_lshlrev_b32_e32 v140, 16, v156
	v_and_b32_e32 v141, 0xffff0000, v156
	v_lshlrev_b32_e32 v142, 16, v157
	v_and_b32_e32 v143, 0xffff0000, v157
	v_mul_f32_e32 v24, v36, v140
	v_mul_f32_e32 v25, v37, v141
	v_mul_f32_e32 v26, v38, v142
	v_mul_f32_e32 v27, v39, v143
	v_cvt_pk_bf16_f32 v144, v24, v25
	v_cvt_pk_bf16_f32 v145, v26, v27
	global_store_dwordx2 v[230:231], v[144:145], off
	v_lshlrev_b32_e32 v140, 16, v158
	v_and_b32_e32 v141, 0xffff0000, v158
	v_lshlrev_b32_e32 v142, 16, v159
	v_and_b32_e32 v143, 0xffff0000, v159
	v_mul_f32_e32 v36, v40, v140
	v_mul_f32_e32 v37, v41, v141
	v_mul_f32_e32 v38, v42, v142
	v_mul_f32_e32 v39, v43, v143
	v_cvt_pk_bf16_f32 v146, v36, v37
; __device__ __forceinline__ unsigned cvtpk(float lo, float hi) { f32x2_t v = {lo, hi}; bf16x2_t b = __builtin_convertvector(v, bf16x2_t); return __builtin_bit_cast(unsigned, b); }
; __device__ __forceinline__ float bflo(unsigned w) { return __uint_as_float(w << 16); }
; __device__ __forceinline__ float bfhi(unsigned w) { return __uint_as_float(w & 0xffff0000u); }
; __device__ __forceinline__ void phase_merge(const Ptrs& p, LAS unsigned char* lds) {
;     ...
;                 for (int m = 0; m < 4; ++m) { const int row = row0 + ai * 128 + wr * 64 + m * 16 + fr;
; #pragma unroll
;                     for (int bj = 0; bj < 2; ++bj)
; #pragma unroll
;                         for (int n = 0; n < 2; ++n) { const int c = col0 + bj * 128 + wc * 32 + n * 16 + fq * 4; const size_t o = (size_t)row * PLD + c;
;                             const u32x2 sa = *(const u32x2*)(pr + o + C_GA); u32x2 sc = sa; if (seg == 0) sc = *(const u32x2*)(pr + o + C_GC);
;                             f32x4 v = acc[ai][bj][m][n];
;                             const float a0 = bflo(sa.x), a1 = bfhi(sa.x), a2 = bflo(sa.y), a3 = bfhi(sa.y);
;                             if (seg == 0) { v[0] *= bflo(sc.x) * __builtin_amdgcn_rcpf(a0); v[1] *= bfhi(sc.x) * __builtin_amdgcn_rcpf(a1); v[2] *= bflo(sc.y) * __builtin_amdgcn_rcpf(a2); v[3] *= bfhi(sc.y) * __builtin_amdgcn_rcpf(a3); }
;                             else { v[0] *= a0; v[1] *= a1; v[2] *= a2; v[3] *= a3; }
;                             acc[ai][bj][m][n] = v;
;                             if (seg == 1) { u32x2 w; w.x = cvtpk(v[0], v[1]); w.y = cvtpk(v[2], v[3]); *(u32x2*)(mg + (size_t)row * D + c) = w; } }
;                     asm volatile("" ::: "memory"); }
	v_cvt_pk_bf16_f32 v147, v38, v39
	global_store_dwordx2 v[230:231], v[146:147], off offset:32
	v_lshlrev_b32_e32 v140, 16, v160
	v_and_b32_e32 v141, 0xffff0000, v160
	v_lshlrev_b32_e32 v142, 16, v161
	v_and_b32_e32 v143, 0xffff0000, v161
	v_mul_f32_e32 v40, v48, v140
	v_mul_f32_e32 v41, v49, v141
	v_mul_f32_e32 v42, v50, v142
	v_mul_f32_e32 v43, v51, v143
	v_cvt_pk_bf16_f32 v144, v40, v41
	v_cvt_pk_bf16_f32 v145, v42, v43
	global_store_dwordx2 v[230:231], v[144:145], off offset:256
	v_lshlrev_b32_e32 v140, 16, v162
	v_and_b32_e32 v141, 0xffff0000, v162
	v_lshlrev_b32_e32 v142, 16, v163
	v_and_b32_e32 v143, 0xffff0000, v163
	v_mul_f32_e32 v48, v56, v140
	v_mul_f32_e32 v49, v57, v141
	v_mul_f32_e32 v50, v58, v142
	v_mul_f32_e32 v51, v59, v143
	v_cvt_pk_bf16_f32 v146, v48, v49
	v_cvt_pk_bf16_f32 v147, v50, v51
	global_store_dwordx2 v[230:231], v[146:147], off offset:288
	v_lshlrev_b32_e32 v140, 16, v164
	v_and_b32_e32 v141, 0xffff0000, v164
	v_lshlrev_b32_e32 v142, 16, v165
	v_and_b32_e32 v143, 0xffff0000, v165
	v_mul_f32_e32 v56, v68, v140
	v_mul_f32_e32 v57, v69, v141
	v_mul_f32_e32 v58, v70, v142
	v_mul_f32_e32 v59, v71, v143
	v_cvt_pk_bf16_f32 v144, v56, v57
	v_cvt_pk_bf16_f32 v145, v58, v59
	global_store_dwordx2 v[232:233], v[144:145], off
	v_lshlrev_b32_e32 v140, 16, v166
	v_and_b32_e32 v141, 0xffff0000, v166
	v_lshlrev_b32_e32 v142, 16, v167
	v_and_b32_e32 v143, 0xffff0000, v167
	v_mul_f32_e32 v68, v72, v140
	v_mul_f32_e32 v69, v73, v141
	v_mul_f32_e32 v70, v74, v142
	v_mul_f32_e32 v71, v75, v143
	v_cvt_pk_bf16_f32 v146, v68, v69
	v_cvt_pk_bf16_f32 v147, v70, v71
	global_store_dwordx2 v[232:233], v[146:147], off offset:32
	v_lshlrev_b32_e32 v140, 16, v168
	v_and_b32_e32 v141, 0xffff0000, v168
	v_lshlrev_b32_e32 v142, 16, v169
	v_and_b32_e32 v143, 0xffff0000, v169
	v_mul_f32_e32 v72, v80, v140
	v_mul_f32_e32 v73, v81, v141
	v_mul_f32_e32 v74, v82, v142
	v_mul_f32_e32 v75, v83, v143
	v_cvt_pk_bf16_f32 v144, v72, v73
	v_cvt_pk_bf16_f32 v145, v74, v75
	global_store_dwordx2 v[232:233], v[144:145], off offset:256
	v_lshlrev_b32_e32 v140, 16, v170
	v_and_b32_e32 v141, 0xffff0000, v170
	v_lshlrev_b32_e32 v142, 16, v171
	v_and_b32_e32 v143, 0xffff0000, v171
	v_mul_f32_e32 v80, v88, v140
	v_mul_f32_e32 v81, v89, v141
	v_mul_f32_e32 v82, v90, v142
	v_mul_f32_e32 v83, v91, v143
	v_cvt_pk_bf16_f32 v146, v80, v81
	v_cvt_pk_bf16_f32 v147, v82, v83
	global_store_dwordx2 v[232:233], v[146:147], off offset:288
	v_lshlrev_b32_e32 v140, 16, v172
	v_and_b32_e32 v141, 0xffff0000, v172
	v_lshlrev_b32_e32 v142, 16, v173
	v_and_b32_e32 v143, 0xffff0000, v173
	v_mul_f32_e32 v88, v100, v140
	v_mul_f32_e32 v89, v101, v141
	v_mul_f32_e32 v90, v102, v142
	v_mul_f32_e32 v91, v103, v143
	v_cvt_pk_bf16_f32 v144, v88, v89
	v_cvt_pk_bf16_f32 v145, v90, v91
	global_store_dwordx2 v[234:235], v[144:145], off
	v_lshlrev_b32_e32 v140, 16, v174
	v_and_b32_e32 v141, 0xffff0000, v174
	v_lshlrev_b32_e32 v142, 16, v175
	v_and_b32_e32 v143, 0xffff0000, v175
	v_mul_f32_e32 v100, v104, v140
	v_mul_f32_e32 v101, v105, v141
	v_mul_f32_e32 v102, v106, v142
	v_mul_f32_e32 v103, v107, v143
	v_cvt_pk_bf16_f32 v146, v100, v101
	v_cvt_pk_bf16_f32 v147, v102, v103
	global_store_dwordx2 v[234:235], v[146:147], off offset:32
	v_lshlrev_b32_e32 v140, 16, v176
	v_and_b32_e32 v141, 0xffff0000, v176
	v_lshlrev_b32_e32 v142, 16, v177
	v_and_b32_e32 v143, 0xffff0000, v177
	v_mul_f32_e32 v104, v112, v140
	v_mul_f32_e32 v105, v113, v141
	v_mul_f32_e32 v106, v114, v142
	v_mul_f32_e32 v107, v115, v143
	v_cvt_pk_bf16_f32 v144, v104, v105
	v_cvt_pk_bf16_f32 v145, v106, v107
	global_store_dwordx2 v[234:235], v[144:145], off offset:256
	v_lshlrev_b32_e32 v140, 16, v178
	v_and_b32_e32 v141, 0xffff0000, v178
	v_lshlrev_b32_e32 v142, 16, v179
	v_and_b32_e32 v143, 0xffff0000, v179
	v_mul_f32_e32 v112, v120, v140
	v_mul_f32_e32 v113, v121, v141
	v_mul_f32_e32 v114, v122, v142
	v_mul_f32_e32 v115, v123, v143
	v_cvt_pk_bf16_f32 v146, v112, v113
	v_cvt_pk_bf16_f32 v147, v114, v115
	global_store_dwordx2 v[234:235], v[146:147], off offset:288
	v_lshlrev_b32_e32 v140, 16, v180
	v_and_b32_e32 v141, 0xffff0000, v180
	v_lshlrev_b32_e32 v142, 16, v181
	v_and_b32_e32 v143, 0xffff0000, v181
	v_mul_f32_e32 v120, v128, v140
	v_mul_f32_e32 v121, v129, v141
	v_mul_f32_e32 v122, v130, v142
	v_mul_f32_e32 v123, v131, v143
	v_cvt_pk_bf16_f32 v144, v120, v121
	v_cvt_pk_bf16_f32 v145, v122, v123
	global_store_dwordx2 v[236:237], v[144:145], off
	v_lshlrev_b32_e32 v140, 16, v182
	v_and_b32_e32 v141, 0xffff0000, v182
	v_lshlrev_b32_e32 v142, 16, v183
	v_and_b32_e32 v143, 0xffff0000, v183
	v_mul_f32_e32 v128, v132, v140
	v_mul_f32_e32 v129, v133, v141
	v_mul_f32_e32 v130, v134, v142
	v_mul_f32_e32 v131, v135, v143
	v_cvt_pk_bf16_f32 v146, v128, v129
	v_cvt_pk_bf16_f32 v147, v130, v131
	global_store_dwordx2 v[236:237], v[146:147], off offset:32
	v_lshlrev_b32_e32 v140, 16, v184
	v_and_b32_e32 v141, 0xffff0000, v184
	v_lshlrev_b32_e32 v142, 16, v185
	v_and_b32_e32 v143, 0xffff0000, v185
	v_mul_f32_e32 v132, v124, v140
	v_mul_f32_e32 v133, v125, v141
	v_mul_f32_e32 v134, v126, v142
	v_mul_f32_e32 v135, v127, v143
	v_cvt_pk_bf16_f32 v144, v132, v133
	v_cvt_pk_bf16_f32 v145, v134, v135
; __device__ __forceinline__ unsigned cvtpk(float lo, float hi) { f32x2_t v = {lo, hi}; bf16x2_t b = __builtin_convertvector(v, bf16x2_t); return __builtin_bit_cast(unsigned, b); }
; __device__ __forceinline__ float bflo(unsigned w) { return __uint_as_float(w << 16); }
; __device__ __forceinline__ float bfhi(unsigned w) { return __uint_as_float(w & 0xffff0000u); }
; __device__ __forceinline__ void phase_merge(const Ptrs& p, LAS unsigned char* lds) {
;     ...
;                 for (int m = 0; m < 4; ++m) { const int row = row0 + ai * 128 + wr * 64 + m * 16 + fr;
; #pragma unroll
;                     for (int bj = 0; bj < 2; ++bj)
; #pragma unroll
;                         for (int n = 0; n < 2; ++n) { const int c = col0 + bj * 128 + wc * 32 + n * 16 + fq * 4; const size_t o = (size_t)row * PLD + c;
;                             const u32x2 sa = *(const u32x2*)(pr + o + C_GA); u32x2 sc = sa; if (seg == 0) sc = *(const u32x2*)(pr + o + C_GC);
;                             f32x4 v = acc[ai][bj][m][n];
;                             const float a0 = bflo(sa.x), a1 = bfhi(sa.x), a2 = bflo(sa.y), a3 = bfhi(sa.y);
;                             if (seg == 0) { v[0] *= bflo(sc.x) * __builtin_amdgcn_rcpf(a0); v[1] *= bfhi(sc.x) * __builtin_amdgcn_rcpf(a1); v[2] *= bflo(sc.y) * __builtin_amdgcn_rcpf(a2); v[3] *= bfhi(sc.y) * __builtin_amdgcn_rcpf(a3); }
;                             else { v[0] *= a0; v[1] *= a1; v[2] *= a2; v[3] *= a3; }
;                             acc[ai][bj][m][n] = v;
;                             if (seg == 1) { u32x2 w; w.x = cvtpk(v[0], v[1]); w.y = cvtpk(v[2], v[3]); *(u32x2*)(mg + (size_t)row * D + c) = w; } }
;                     asm volatile("" ::: "memory"); }
	global_store_dwordx2 v[236:237], v[144:145], off offset:256
	v_lshlrev_b32_e32 v140, 16, v186
	v_and_b32_e32 v141, 0xffff0000, v186
	v_lshlrev_b32_e32 v142, 16, v187
	v_and_b32_e32 v143, 0xffff0000, v187
	v_mul_f32_e32 v124, v116, v140
	v_mul_f32_e32 v125, v117, v141
	v_mul_f32_e32 v126, v118, v142
	v_mul_f32_e32 v127, v119, v143
	v_cvt_pk_bf16_f32 v146, v124, v125
	v_cvt_pk_bf16_f32 v147, v126, v127
	global_store_dwordx2 v[236:237], v[146:147], off offset:288
	v_lshlrev_b32_e32 v140, 16, v188
	v_and_b32_e32 v141, 0xffff0000, v188
	v_lshlrev_b32_e32 v142, 16, v189
	v_and_b32_e32 v143, 0xffff0000, v189
	v_mul_f32_e32 v116, v108, v140
	v_mul_f32_e32 v117, v109, v141
	v_mul_f32_e32 v118, v110, v142
	v_mul_f32_e32 v119, v111, v143
	v_cvt_pk_bf16_f32 v144, v116, v117
	v_cvt_pk_bf16_f32 v145, v118, v119
	global_store_dwordx2 v[238:239], v[144:145], off
	v_lshlrev_b32_e32 v140, 16, v190
	v_and_b32_e32 v141, 0xffff0000, v190
	v_lshlrev_b32_e32 v142, 16, v191
	v_and_b32_e32 v143, 0xffff0000, v191
	v_mul_f32_e32 v108, v96, v140
	v_mul_f32_e32 v109, v97, v141
	v_mul_f32_e32 v110, v98, v142
	v_mul_f32_e32 v111, v99, v143
	v_cvt_pk_bf16_f32 v146, v108, v109
	v_cvt_pk_bf16_f32 v147, v110, v111
	global_store_dwordx2 v[238:239], v[146:147], off offset:32
	v_lshlrev_b32_e32 v140, 16, v192
	v_and_b32_e32 v141, 0xffff0000, v192
	v_lshlrev_b32_e32 v142, 16, v193
	v_and_b32_e32 v143, 0xffff0000, v193
	v_mul_f32_e32 v96, v92, v140
	v_mul_f32_e32 v97, v93, v141
	v_mul_f32_e32 v98, v94, v142
	v_mul_f32_e32 v99, v95, v143
	v_cvt_pk_bf16_f32 v144, v96, v97
	v_cvt_pk_bf16_f32 v145, v98, v99
	global_store_dwordx2 v[238:239], v[144:145], off offset:256
	v_lshlrev_b32_e32 v140, 16, v194
	v_and_b32_e32 v141, 0xffff0000, v194
	v_lshlrev_b32_e32 v142, 16, v195
	v_and_b32_e32 v143, 0xffff0000, v195
	v_mul_f32_e32 v92, v84, v140
	v_mul_f32_e32 v93, v85, v141
	v_mul_f32_e32 v94, v86, v142
	v_mul_f32_e32 v95, v87, v143
	v_cvt_pk_bf16_f32 v146, v92, v93
	v_cvt_pk_bf16_f32 v147, v94, v95
	global_store_dwordx2 v[238:239], v[146:147], off offset:288
	v_lshlrev_b32_e32 v140, 16, v196
	v_and_b32_e32 v141, 0xffff0000, v196
	v_lshlrev_b32_e32 v142, 16, v197
	v_and_b32_e32 v143, 0xffff0000, v197
	v_mul_f32_e32 v84, v76, v140
	v_mul_f32_e32 v85, v77, v141
	v_mul_f32_e32 v86, v78, v142
	v_mul_f32_e32 v87, v79, v143
	v_cvt_pk_bf16_f32 v144, v84, v85
	v_cvt_pk_bf16_f32 v145, v86, v87
	global_store_dwordx2 v[240:241], v[144:145], off
	v_lshlrev_b32_e32 v140, 16, v198
	v_and_b32_e32 v141, 0xffff0000, v198
	v_lshlrev_b32_e32 v142, 16, v199
	v_and_b32_e32 v143, 0xffff0000, v199
	v_mul_f32_e32 v76, v64, v140
	v_mul_f32_e32 v77, v65, v141
	v_mul_f32_e32 v78, v66, v142
	v_mul_f32_e32 v79, v67, v143
	v_cvt_pk_bf16_f32 v146, v76, v77
	v_cvt_pk_bf16_f32 v147, v78, v79
	global_store_dwordx2 v[240:241], v[146:147], off offset:32
	v_lshlrev_b32_e32 v140, 16, v200
	v_and_b32_e32 v141, 0xffff0000, v200
	v_lshlrev_b32_e32 v142, 16, v201
	v_and_b32_e32 v143, 0xffff0000, v201
	v_mul_f32_e32 v64, v60, v140
	v_mul_f32_e32 v65, v61, v141
	v_mul_f32_e32 v66, v62, v142
	v_mul_f32_e32 v67, v63, v143
	v_cvt_pk_bf16_f32 v144, v64, v65
	v_cvt_pk_bf16_f32 v145, v66, v67
	global_store_dwordx2 v[240:241], v[144:145], off offset:256
	v_lshlrev_b32_e32 v140, 16, v202
	v_and_b32_e32 v141, 0xffff0000, v202
	v_lshlrev_b32_e32 v142, 16, v203
	v_and_b32_e32 v143, 0xffff0000, v203
	v_mul_f32_e32 v60, v52, v140
	v_mul_f32_e32 v61, v53, v141
	v_mul_f32_e32 v62, v54, v142
	v_mul_f32_e32 v63, v55, v143
	v_cvt_pk_bf16_f32 v146, v60, v61
	v_cvt_pk_bf16_f32 v147, v62, v63
	global_store_dwordx2 v[240:241], v[146:147], off offset:288
	v_lshlrev_b32_e32 v140, 16, v204
	v_and_b32_e32 v141, 0xffff0000, v204
	v_lshlrev_b32_e32 v142, 16, v205
	v_and_b32_e32 v143, 0xffff0000, v205
	v_mul_f32_e32 v52, v44, v140
	v_mul_f32_e32 v53, v45, v141
	v_mul_f32_e32 v54, v46, v142
	v_mul_f32_e32 v55, v47, v143
	v_cvt_pk_bf16_f32 v144, v52, v53
	v_cvt_pk_bf16_f32 v145, v54, v55
	global_store_dwordx2 v[242:243], v[144:145], off
	v_lshlrev_b32_e32 v140, 16, v206
	v_and_b32_e32 v141, 0xffff0000, v206
	v_lshlrev_b32_e32 v142, 16, v207
	v_and_b32_e32 v143, 0xffff0000, v207
	v_mul_f32_e32 v44, v32, v140
	v_mul_f32_e32 v45, v33, v141
	v_mul_f32_e32 v46, v34, v142
	v_mul_f32_e32 v47, v35, v143
	v_cvt_pk_bf16_f32 v146, v44, v45
	v_cvt_pk_bf16_f32 v147, v46, v47
	global_store_dwordx2 v[242:243], v[146:147], off offset:32
	v_lshlrev_b32_e32 v140, 16, v208
	v_and_b32_e32 v141, 0xffff0000, v208
	v_lshlrev_b32_e32 v142, 16, v209
	v_and_b32_e32 v143, 0xffff0000, v209
	v_mul_f32_e32 v32, v28, v140
	v_mul_f32_e32 v33, v29, v141
	v_mul_f32_e32 v34, v30, v142
	v_mul_f32_e32 v35, v31, v143
	v_cvt_pk_bf16_f32 v144, v32, v33
	v_cvt_pk_bf16_f32 v145, v34, v35
	global_store_dwordx2 v[242:243], v[144:145], off offset:256
	v_lshlrev_b32_e32 v140, 16, v210
	v_and_b32_e32 v141, 0xffff0000, v210
	v_lshlrev_b32_e32 v142, 16, v211
	v_and_b32_e32 v143, 0xffff0000, v211
	v_mul_f32_e32 v28, v20, v140
	v_mul_f32_e32 v29, v21, v141
	v_mul_f32_e32 v30, v22, v142
	v_mul_f32_e32 v31, v23, v143
	v_cvt_pk_bf16_f32 v146, v28, v29
	v_cvt_pk_bf16_f32 v147, v30, v31
	global_store_dwordx2 v[242:243], v[146:147], off offset:288
	s_branch .LBB0_510
